# baseline (speedup 1.0000x reference)
.LBB1_46:
	s_lshl_b64 s[98:99], s[30:31], 17
	s_lshl_b64 s[0:1], s[8:9], 6
	s_lshl_b64 s[18:19], s[98:99], 1
	s_add_u32 s8, s48, s18
	s_addc_u32 s9, s49, s19
	s_lshl_b64 s[0:1], s[0:1], 4
	s_add_u32 s0, s8, s0
	s_addc_u32 s1, s9, s1
	v_lshl_add_u64 v[124:125], s[0:1], 0, v[98:99]
	v_add_co_u32_e32 v152, vcc, s3, v124
	s_nop 1
	v_addc_co_u32_e32 v153, vcc, 0, v125, vcc
	global_load_dwordx4 v[124:127], v98, s[0:1]
	global_load_dwordx4 v[128:131], v98, s[0:1] offset:1024
	global_load_dwordx4 v[132:135], v[152:153], off
	global_load_dwordx4 v[136:139], v[152:153], off offset:1024
	global_load_dwordx4 v[140:143], v98, s[0:1] offset:2048
	global_load_dwordx4 v[144:147], v98, s[0:1] offset:3072
	global_load_dwordx4 v[148:151], v[152:153], off offset:2048
	s_nop 0
	global_load_dwordx4 v[152:155], v[152:153], off offset:3072
	s_waitcnt vmcnt(5)
	v_mfma_f32_16x16x32_f16 v[156:159], v[2:5], v[132:135], 0
	s_lshl_b32 s0, s20, 12
	s_add_i32 s0, s0, 0
	v_lshl_add_u32 v98, v122, 4, s0
	v_mfma_f32_16x16x32_f16 v[160:163], v[10:13], v[132:135], 0
	v_add_u32_e32 v98, 0x10000, v98
	v_mov_b32_e32 v194, 0
	v_mfma_f32_16x16x32_f16 v[132:135], v[18:21], v[132:135], 0
	v_mfma_f32_16x16x32_f16 v[164:167], v[2:5], v[124:127], 0
	v_mfma_f32_16x16x32_f16 v[168:171], v[10:13], v[124:127], 0
	v_mfma_f32_16x16x32_f16 v[124:127], v[18:21], v[124:127], 0
	s_waitcnt vmcnt(4)
	v_mfma_f32_16x16x32_f16 v[156:159], v[26:29], v[136:139], v[156:159]
	v_mfma_f32_16x16x32_f16 v[160:163], v[34:37], v[136:139], v[160:163]
	v_mfma_f32_16x16x32_f16 v[132:135], v[42:45], v[136:139], v[132:135]
	v_mfma_f32_16x16x32_f16 v[136:139], v[26:29], v[128:131], v[164:167]
	v_mfma_f32_16x16x32_f16 v[164:167], v[34:37], v[128:131], v[168:171]
	v_mfma_f32_16x16x32_f16 v[124:127], v[42:45], v[128:131], v[124:127]
	s_waitcnt vmcnt(1)
	v_mfma_f32_16x16x32_f16 v[128:131], v[50:53], v[148:151], v[156:159]
	v_mfma_f32_16x16x32_f16 v[136:139], v[50:53], v[140:143], v[136:139]
	v_mfma_f32_16x16x32_f16 v[156:159], v[58:61], v[148:151], v[160:163]
	v_mfma_f32_16x16x32_f16 v[132:135], v[66:69], v[148:151], v[132:135]
	v_mfma_f32_16x16x32_f16 v[148:151], v[58:61], v[140:143], v[164:167]
	s_waitcnt vmcnt(0)
	v_mfma_f32_16x16x32_f16 v[128:131], v[74:77], v[152:155], v[128:131]
	v_mfma_f32_16x16x32_f16 v[136:139], v[74:77], v[144:147], v[136:139]
	v_mfma_f32_16x16x32_f16 v[124:127], v[66:69], v[140:143], v[124:127]
	v_mfma_f32_16x16x32_f16 v[140:143], v[82:85], v[152:155], v[156:159]
	s_nop 5
	v_fma_f32 v138, v130, s92, v138
	v_fma_f32 v139, v131, s92, v139
	v_pk_fma_f32 v[136:137], v[128:129], s[92:93], v[136:137] op_sel_hi:[1,0,1]
	v_pk_add_f32 v[116:117], v[116:117], v[138:139]
	v_mfma_f32_16x16x32_f16 v[128:131], v[82:85], v[144:147], v[148:151]
	v_add_f32_e64 v114, v114, v136
	v_add_f32_e64 v115, v115, v137
	v_mfma_f32_16x16x32_f16 v[124:127], v[90:93], v[144:147], v[124:127]
	s_nop 4
	v_fma_f32 v136, v142, s92, v130
	v_fma_f32 v137, v143, s92, v131
	v_mfma_f32_16x16x32_f16 v[130:133], v[90:93], v[152:155], v[132:135]
	v_fma_f32 v128, v140, s92, v128
	v_fma_f32 v129, v141, s92, v129
	v_pk_add_f32 v[112:113], v[112:113], v[136:137]
	v_pk_add_f32 v[110:111], v[110:111], v[128:129]
	s_nop 3
	v_pk_fma_f32 v[126:127], v[132:133], s[92:93], v[126:127] op_sel_hi:[1,0,1]
	v_pk_fma_f32 v[124:125], v[130:131], s[92:93], v[124:125] op_sel_hi:[1,0,1]
	ds_write_b128 v98, v[114:117]
	ds_write_b128 v98, v[110:113] offset:1024
	ds_write_b128 v98, v[124:127] offset:2048
	ds_write_b128 v98, v[104:107] offset:3072
	s_waitcnt lgkmcnt(0)
	s_barrier
	s_and_saveexec_b64 s[0:1], s[4:5]
	s_cbranch_execz .LBB1_48
	v_and_b32_e32 v98, 0xfc, v179
	s_add_i32 s4, 0, 0x10000
	v_lshlrev_b32_e32 v98, 2, v98
	v_lshlrev_b32_e32 v104, 2, v121
	v_add3_u32 v121, s4, v98, v104
	v_lshl_add_u32 v126, v101, 2, 0
	v_add_u32_e32 v129, 0x18580, v126
	ds_read2st64_b32 v[130:131], v121 offset1:4
	ds_read2st64_b32 v[132:133], v121 offset0:16 offset1:20
	ds_read2st64_b32 v[134:135], v121 offset0:32 offset1:36
	ds_read2st64_b32 v[136:137], v121 offset0:48 offset1:52
	ds_read2st64_b32 v[138:139], v121 offset0:64 offset1:68
	ds_read2st64_b32 v[140:141], v121 offset0:80 offset1:84
	ds_read2st64_b32 v[142:143], v121 offset0:96 offset1:100
	ds_read2st64_b32 v[144:145], v121 offset0:112 offset1:116
	ds_read2_b32 v[146:147], v129 offset1:16
	ds_read2st64_b32 v[148:149], v121 offset0:8 offset1:12
	ds_read2st64_b32 v[150:151], v121 offset0:24 offset1:28
	ds_read2st64_b32 v[152:153], v121 offset0:40 offset1:44
	ds_read2st64_b32 v[154:155], v121 offset0:56 offset1:60
	ds_read2st64_b32 v[156:157], v121 offset0:72 offset1:76
	ds_read2st64_b32 v[158:159], v121 offset0:88 offset1:92
	v_lshlrev_b32_e32 v103, 5, v103
	s_add_i32 s4, 0, 0x18000
	v_lshlrev_b32_e32 v101, 1, v101
	v_add3_u32 v101, s4, v103, v101
	s_waitcnt lgkmcnt(6)
	v_add_f32_e32 v106, 0, v130
	v_add_f32_e32 v114, 0, v131
	v_add_f32_e32 v106, v106, v132
	v_add_f32_e32 v114, v114, v133
	v_add_f32_e32 v106, v106, v134
	v_add_f32_e32 v114, v114, v135
	v_add_f32_e32 v106, v106, v136
	v_add_f32_e32 v114, v114, v137
	v_add_f32_e32 v106, v106, v138
	v_add_f32_e32 v114, v114, v139
	v_add_f32_e32 v106, v106, v140
	v_add_f32_e32 v114, v114, v141
	v_add_f32_e32 v106, v106, v142
	v_add_f32_e32 v114, v114, v143
	v_add_f32_e32 v106, v106, v144
	v_add_f32_e32 v114, v114, v145
	ds_read2st64_b32 v[160:161], v121 offset0:104 offset1:108
	ds_read2st64_b32 v[162:163], v121 offset0:120 offset1:124
	ds_read2_b32 v[164:165], v129 offset0:32 offset1:48
	v_add_f32_e32 v106, v119, v106
	v_add_f32_e32 v106, v106, v146
	v_mul_f32_e32 v106, 0xbfb8aa3b, v106
	v_exp_f32_e32 v106, v106
	v_add_f32_e32 v114, v108, v114
	v_add_f32_e32 v114, v114, v147
	v_mul_f32_e32 v114, 0xbfb8aa3b, v114
	v_exp_f32_e32 v108, v114
	v_add_f32_e32 v106, 1.0, v106
	v_rcp_f32_e32 v128, v106
	s_waitcnt lgkmcnt(0)
	v_add_f32_e32 v104, 0, v148
	v_add_f32_e32 v105, 0, v149
	v_add_f32_e32 v104, v104, v150
	v_add_f32_e32 v105, v105, v151
	v_add_f32_e32 v104, v104, v152
	v_add_f32_e32 v105, v105, v153
	v_add_f32_e32 v104, v104, v154
	v_add_f32_e32 v105, v105, v155
	v_add_f32_e32 v104, v104, v156
	v_add_f32_e32 v105, v105, v157
	v_add_f32_e32 v104, v104, v158
	v_add_f32_e32 v105, v105, v159
	v_add_f32_e32 v104, v104, v160
	v_add_f32_e32 v105, v105, v161
	v_add_f32_e32 v104, v104, v162
	v_add_f32_e32 v105, v163, v105
	v_add_f32_e32 v104, v120, v104
	v_add_f32_e32 v104, v104, v164
	v_add_f32_e32 v105, v105, v165
	s_nop 0
	v_fmac_f32_e32 v104, v105, v128
	v_add_f32_e32 v98, v104, v104
	v_mul_f32_e32 v98, 0x3fb8aa3b, v98
	v_exp_f32_e32 v98, v98
	v_add_f32_e32 v104, 1.0, v108
	v_rcp_f32_e32 v104, v104
	v_add_f32_e32 v98, 1.0, v98
	v_rcp_f32_e32 v98, v98
	v_sub_f32_e32 v119, 1.0, v104
	v_fma_f32 v105, v98, -2.0, 1.0
	v_pk_mul_f32 v[104:105], v[118:119], v[104:105]
	s_nop 0
	v_add_f32_e32 v194, v104, v105
	v_cvt_f16_f32_e32 v98, v194
	v_cvt_f32_f16_e32 v104, v98
	v_sub_f32_e32 v104, v194, v104
	v_fma_mixlo_f16 v104, v104, s94, 0
	ds_write_b16 v101, v98
	ds_write_b16 v101, v104 offset:512

.LBB1_67:
	s_lshl_b64 s[18:19], s[18:19], 6
	v_cmp_gt_i32_e64 s[0:1], s11, v179
	s_lshl_b64 s[18:19], s[18:19], 4
	s_add_u32 s4, s4, s18
	s_addc_u32 s5, s5, s19
	v_lshl_add_u64 v[118:119], s[4:5], 0, v[98:99]
	v_add_co_u32_e32 v146, vcc, s3, v118
	s_nop 1
	v_addc_co_u32_e32 v147, vcc, 0, v119, vcc
	global_load_dwordx4 v[118:121], v98, s[4:5]
	global_load_dwordx4 v[122:125], v98, s[4:5] offset:1024
	global_load_dwordx4 v[126:129], v[146:147], off
	global_load_dwordx4 v[130:133], v[146:147], off offset:1024
	global_load_dwordx4 v[134:137], v98, s[4:5] offset:2048
	global_load_dwordx4 v[138:141], v98, s[4:5] offset:3072
	global_load_dwordx4 v[142:145], v[146:147], off offset:2048
	s_nop 0
	global_load_dwordx4 v[146:149], v[146:147], off offset:3072
	s_waitcnt vmcnt(5)
	v_mfma_f32_16x16x32_f16 v[150:153], v[6:9], v[126:129], 0
	s_lshl_b32 s4, s9, 12
	s_add_i32 s4, s4, 0
	v_add_u32_e32 v98, s4, v98
	v_mfma_f32_16x16x32_f16 v[154:157], v[14:17], v[126:129], 0
	v_add_u32_e32 v98, 0x10000, v98
	v_mov_b32_e32 v195, 0
	v_mfma_f32_16x16x32_f16 v[126:129], v[22:25], v[126:129], 0
	v_mfma_f32_16x16x32_f16 v[158:161], v[6:9], v[118:121], 0
	v_mfma_f32_16x16x32_f16 v[162:165], v[14:17], v[118:121], 0
	v_mfma_f32_16x16x32_f16 v[118:121], v[22:25], v[118:121], 0
	s_waitcnt vmcnt(4)
	v_mfma_f32_16x16x32_f16 v[150:153], v[30:33], v[130:133], v[150:153]
	v_mfma_f32_16x16x32_f16 v[154:157], v[38:41], v[130:133], v[154:157]
	v_mfma_f32_16x16x32_f16 v[126:129], v[46:49], v[130:133], v[126:129]
	v_mfma_f32_16x16x32_f16 v[130:133], v[30:33], v[122:125], v[158:161]
	v_mfma_f32_16x16x32_f16 v[158:161], v[38:41], v[122:125], v[162:165]
	v_mfma_f32_16x16x32_f16 v[118:121], v[46:49], v[122:125], v[118:121]
	s_waitcnt vmcnt(1)
	v_mfma_f32_16x16x32_f16 v[122:125], v[54:57], v[142:145], v[150:153]
	v_mfma_f32_16x16x32_f16 v[130:133], v[54:57], v[134:137], v[130:133]
	v_mfma_f32_16x16x32_f16 v[150:153], v[62:65], v[142:145], v[154:157]
	v_mfma_f32_16x16x32_f16 v[126:129], v[70:73], v[142:145], v[126:129]
	v_mfma_f32_16x16x32_f16 v[142:145], v[62:65], v[134:137], v[158:161]
	s_waitcnt vmcnt(0)
	v_mfma_f32_16x16x32_f16 v[122:125], v[78:81], v[146:149], v[122:125]
	v_mfma_f32_16x16x32_f16 v[130:133], v[78:81], v[138:141], v[130:133]
	v_mfma_f32_16x16x32_f16 v[118:121], v[70:73], v[134:137], v[118:121]
	v_mfma_f32_16x16x32_f16 v[134:137], v[86:89], v[146:149], v[150:153]
	s_nop 5
	v_fma_f32 v132, v124, s92, v132
	v_fma_f32 v133, v125, s92, v133
	v_pk_fma_f32 v[130:131], v[122:123], s[92:93], v[130:131] op_sel_hi:[1,0,1]
	v_pk_add_f32 v[116:117], v[116:117], v[132:133]
	v_mfma_f32_16x16x32_f16 v[122:125], v[86:89], v[138:141], v[142:145]
	v_add_f32_e64 v114, v114, v130
	v_add_f32_e64 v115, v115, v131
	v_mfma_f32_16x16x32_f16 v[118:121], v[94:97], v[138:141], v[118:121]
	s_nop 4
	v_fma_f32 v130, v136, s92, v124
	v_fma_f32 v131, v137, s92, v125
	v_mfma_f32_16x16x32_f16 v[124:127], v[94:97], v[146:149], v[126:129]
	v_fma_f32 v122, v134, s92, v122
	v_fma_f32 v123, v135, s92, v123
	v_pk_add_f32 v[112:113], v[112:113], v[130:131]
	v_pk_add_f32 v[110:111], v[110:111], v[122:123]
	s_nop 3
	v_pk_fma_f32 v[120:121], v[126:127], s[92:93], v[120:121] op_sel_hi:[1,0,1]
	v_pk_fma_f32 v[118:119], v[124:125], s[92:93], v[118:119] op_sel_hi:[1,0,1]
	ds_write_b128 v98, v[114:117]
	ds_write_b128 v98, v[110:113] offset:1024
	ds_write_b128 v98, v[118:121] offset:2048
	ds_write_b128 v98, v[104:107] offset:3072
	s_waitcnt lgkmcnt(0)
	s_barrier
	s_and_saveexec_b64 s[4:5], s[0:1]
	s_cbranch_execz .LBB1_69
	v_and_b32_e32 v98, 3, v179
	v_and_b32_e32 v101, 0xfc, v179
	s_add_i32 s0, 0, 0x10000
	v_lshlrev_b32_e32 v101, 2, v101
	v_lshlrev_b32_e32 v103, 2, v98
	v_add3_u32 v101, s0, v101, v103
	v_lshrrev_b32_e32 v103, 4, v179
	v_and_or_b32 v103, v103, 12, v98
	v_lshl_add_u32 v122, v103, 2, 0
	v_add_u32_e32 v124, 0x18680, v122
	ds_read2st64_b32 v[130:131], v101 offset1:4
	ds_read2st64_b32 v[132:133], v101 offset0:16 offset1:20
	ds_read2st64_b32 v[134:135], v101 offset0:32 offset1:36
	ds_read2st64_b32 v[136:137], v101 offset0:48 offset1:52
	ds_read2st64_b32 v[138:139], v101 offset0:64 offset1:68
	ds_read2st64_b32 v[140:141], v101 offset0:80 offset1:84
	ds_read2st64_b32 v[142:143], v101 offset0:96 offset1:100
	ds_read2st64_b32 v[144:145], v101 offset0:112 offset1:116
	ds_read2_b32 v[146:147], v124 offset1:16
	ds_read2st64_b32 v[148:149], v101 offset0:8 offset1:12
	ds_read2st64_b32 v[150:151], v101 offset0:24 offset1:28
	ds_read2st64_b32 v[152:153], v101 offset0:40 offset1:44
	ds_read2st64_b32 v[154:155], v101 offset0:56 offset1:60
	ds_read2st64_b32 v[156:157], v101 offset0:72 offset1:76
	ds_read2st64_b32 v[158:159], v101 offset0:88 offset1:92
	s_add_i32 s0, 0, 0x18000
	s_waitcnt lgkmcnt(6)
	v_add_f32_e32 v106, 0, v130
	v_add_f32_e32 v108, 0, v131
	v_add_f32_e32 v106, v106, v132
	v_add_f32_e32 v108, v108, v133
	v_add_f32_e32 v106, v106, v134
	v_add_f32_e32 v108, v108, v135
	v_add_f32_e32 v106, v106, v136
	v_add_f32_e32 v108, v108, v137
	v_add_f32_e32 v106, v106, v138
	v_add_f32_e32 v108, v108, v139
	v_add_f32_e32 v106, v106, v140
	v_add_f32_e32 v108, v108, v141
	v_add_f32_e32 v106, v106, v142
	v_add_f32_e32 v108, v108, v143
	v_add_f32_e32 v106, v106, v144
	v_add_f32_e32 v108, v108, v145
	ds_read2st64_b32 v[160:161], v101 offset0:104 offset1:108
	ds_read2st64_b32 v[162:163], v101 offset0:120 offset1:124
	ds_read2_b32 v[164:165], v124 offset0:32 offset1:48
	v_add_f32_e32 v106, 0, v106
	v_add_f32_e32 v106, v106, v146
	v_mul_f32_e32 v106, 0xbfb8aa3b, v106
	v_exp_f32_e32 v106, v106
	v_add_f32_e32 v114, 0, v108
	v_add_f32_e32 v114, v114, v147
	v_mul_f32_e32 v114, 0xbfb8aa3b, v114
	v_exp_f32_e32 v108, v114
	v_add_f32_e32 v101, 1.0, v106
	v_rcp_f32_e32 v101, v101
	s_waitcnt lgkmcnt(0)
	v_add_f32_e32 v104, 0, v148
	v_add_f32_e32 v105, 0, v149
	v_add_f32_e32 v104, v104, v150
	v_add_f32_e32 v105, v105, v151
	v_add_f32_e32 v104, v104, v152
	v_add_f32_e32 v105, v105, v153
	v_add_f32_e32 v104, v104, v154
	v_add_f32_e32 v105, v105, v155
	v_add_f32_e32 v104, v104, v156
	v_add_f32_e32 v105, v105, v157
	v_add_f32_e32 v104, v104, v158
	v_add_f32_e32 v105, v105, v159
	v_add_f32_e32 v104, v104, v160
	v_add_f32_e32 v105, v105, v161
	v_add_f32_e32 v104, v104, v162
	v_add_f32_e32 v104, v104, v99
	v_add_f32_e32 v105, v105, v163
	v_lshlrev_b32_e32 v103, 1, v103
	v_add_f32_e32 v104, v104, v164
	v_add_f32_e32 v105, v105, v165
	s_nop 0
	v_fmac_f32_e32 v104, v105, v101
	v_add_f32_e32 v98, v104, v104
	v_mul_f32_e32 v98, 0x3fb8aa3b, v98
	v_exp_f32_e32 v98, v98
	v_add_f32_e32 v101, 1.0, v108
	v_rcp_f32_e32 v104, v101
	v_add_f32_e32 v98, 1.0, v98
	v_rcp_f32_e32 v98, v98
	v_sub_f32_e32 v101, 1.0, v104
	v_fma_f32 v105, v98, -2.0, 1.0
	v_pk_mul_f32 v[100:101], v[100:101], v[104:105]
	s_nop 0
	v_add_f32_e32 v195, v100, v101
	v_cvt_f16_f32_e32 v98, v195
	v_lshlrev_b32_e32 v101, 3, v179
	v_and_b32_e32 v101, 0x1e0, v101
	v_add3_u32 v101, s0, v101, v103
	v_cvt_f32_f16_e32 v100, v98
	v_sub_f32_e32 v100, v195, v100
	v_fma_mixlo_f16 v100, v100, s94, 0
	ds_write_b16 v101, v98
	ds_write_b16 v101, v100 offset:512
